# P2: streaming q/logf/i loads marked nt (read once) so the attention Q/K/V written in P1 are not evicted before P3
# baseline (speedup 1.0000x reference)
; DI int opaque_tid() { int t = threadIdx.x; asm volatile("" : "+v"(t)); return t; }
; DI void p2_hgrn_roles(Frame& F, ArgsP A) {
;     ...
;     for (int item = F.vcu; item < 256; item += F.G) {
;         const int bh = item >> 1, vhalf = item & 1, b = bh >> 4, h = bh & 15;
;         const size_t rb = (size_t)b * SEQ * D;
;         unsigned CR[72];
;         f32x16 S0, S1;
; #pragma unroll
;         for (int i = 0; i < 72; ++i) CR[i] = 0u;
; #pragma unroll
;         for (int i = 0; i < 16; ++i) { S0[i] = 0.f; S1[i] = 0.f; }
;     ...
;         if (prep) {
;             const int pt = opaque_tid() & 255, k2 = pt & 63, tgp = pt >> 6, v64 = pt & 63;
;             const bf16_t* qp = (const bf16_t*)(A->ws + WS_QA) + rb + (size_t)(8 * tgp) * D + h * 128 + 2 * k2; const bf16_t* fp = (const bf16_t*)(A->ws + WS_LF) + rb + (size_t)(8 * tgp) * D + h * 128 + 2 * k2;
;             const bf16_t* ip = (const bf16_t*)(A->ws + WS_IA) + rb + (size_t)(8 * tgp) * D + h * 128 + vhalf * 64 + v64;
;             h_load8<0>(CR, qp, fp, ip, 0); h_load8<1>(CR, qp, fp, ip, 1); h_load8<2>(CR, qp, fp, ip, 2); h_totals8<0>(CR, lds, tgp, k2);
.LBB0_405:
	s_ashr_i32 s6, s95, 5
	s_ashr_i32 s7, s6, 31
	s_bfe_u32 s9, s95, 0x40001
	s_and_b32 s8, s95, 1
	s_lshl_b64 s[52:53], s[6:7], 22
	s_and_b64 vcc, exec, s[36:37]
	s_waitcnt vmcnt(2)
	v_mov_b32_e32 v180, v3
	v_mov_b32_e32 v169, v3
	v_mov_b32_e32 v165, v3
	v_mov_b32_e32 v153, v3
	v_mov_b32_e32 v148, v3
	v_mov_b32_e32 v146, v3
	v_mov_b32_e32 v127, v3
	v_mov_b32_e32 v125, v3
	v_mov_b32_e32 v175, v3
	v_mov_b32_e32 v172, v3
	v_mov_b32_e32 v167, v3
	v_mov_b32_e32 v155, v3
	v_mov_b32_e32 v157, v3
	v_mov_b32_e32 v140, v3
	v_mov_b32_e32 v131, v3
	v_mov_b32_e32 v129, v3
	s_waitcnt vmcnt(0)
	v_mov_b32_e32 v182, v3
	v_mov_b32_e32 v178, v3
	v_mov_b32_e32 v162, v3
	v_mov_b32_e32 v160, v3
	v_mov_b32_e32 v151, v3
	v_mov_b32_e32 v134, v3
	v_mov_b32_e32 v138, v3
	v_mov_b32_e32 v135, v3
	v_mov_b32_e32 v181, v3
	v_mov_b32_e32 v170, v3
	v_mov_b32_e32 v166, v3
	v_mov_b32_e32 v154, v3
	v_mov_b32_e32 v149, v3
	v_mov_b32_e32 v147, v3
	v_mov_b32_e32 v128, v3
	v_mov_b32_e32 v126, v3
	v_mov_b32_e32 v176, v3
	v_mov_b32_e32 v173, v3
	v_mov_b32_e32 v168, v3
	v_mov_b32_e32 v156, v3
	v_mov_b32_e32 v158, v3
	v_mov_b32_e32 v141, v3
	v_mov_b32_e32 v132, v3
	v_mov_b32_e32 v130, v3
	v_mov_b32_e32 v183, v3
	v_mov_b32_e32 v179, v3
	v_mov_b32_e32 v163, v3
	v_mov_b32_e32 v161, v3
	v_mov_b32_e32 v152, v3
	v_mov_b32_e32 v136, v3
	v_mov_b32_e32 v139, v3
	v_mov_b32_e32 v137, v3
	v_mov_b32_e32 v187, v3
	v_mov_b32_e32 v190, v3
	v_mov_b32_e32 v192, v3
	v_mov_b32_e32 v191, v3
	v_mov_b32_e32 v186, v3
	v_mov_b32_e32 v188, v3
	v_mov_b32_e32 v185, v3
	v_mov_b32_e32 v189, v3
	v_mov_b32_e32 v174, v3
	v_mov_b32_e32 v171, v3
	v_mov_b32_e32 v164, v3
	v_mov_b32_e32 v150, v3
	v_mov_b32_e32 v144, v3
	v_mov_b32_e32 v133, v3
	v_mov_b32_e32 v122, v3
	v_mov_b32_e32 v121, v3
	v_mov_b32_e32 v177, v3
	v_mov_b32_e32 v184, v3
	v_mov_b32_e32 v159, v3
	v_mov_b32_e32 v145, v3
	v_mov_b32_e32 v143, v3
	v_mov_b32_e32 v123, v3
	v_mov_b32_e32 v124, v3
	v_mov_b32_e32 v142, v3
	s_cbranch_vccnz .LBB0_407
	v_lshlrev_b32_e32 v200, 9, v0
	v_and_b32_e32 v200, 0x18000, v200
	v_and_b32_e32 v201, 63, v0
	v_lshl_or_b32 v208, v201, 1, v200
	v_lshl_or_b32 v200, v201, 2, v200
	v_cndmask_b32_e64 v201, 0, 1, s[44:45]
	v_lshl_add_u32 v208, v201, 7, v208
	v_add_u32_e32 v201, 0x1000, v200
	v_add_u32_e32 v202, 0x2000, v200
	v_add_u32_e32 v203, 0x3000, v200
	v_add_u32_e32 v204, 0x4000, v200
	v_add_u32_e32 v205, 0x5000, v200
	v_add_u32_e32 v206, 0x6000, v200
	v_add_u32_e32 v207, 0x7000, v200
	v_add_u32_e32 v209, 0x1000, v208
	v_add_u32_e32 v210, 0x2000, v208
	v_add_u32_e32 v211, 0x3000, v208
	v_add_u32_e32 v212, 0x4000, v208
	v_add_u32_e32 v213, 0x5000, v208
	v_add_u32_e32 v214, 0x6000, v208
	v_add_u32_e32 v215, 0x7000, v208
	v_mov_b32_e32 v2, v0
	s_load_dwordx2 s[4:5], s[40:41], 0x98
	s_lshl_b64 s[10:11], s[52:53], 1
	s_lshl_b32 s48, s9, 8
	v_bfe_u32 v77, v2, 6, 2
	v_and_b32_e32 v76, 63, v2
	s_waitcnt lgkmcnt(0)
	s_add_u32 s4, s4, s10
	v_lshlrev_b32_e32 v2, 15, v77
	s_addc_u32 s5, s5, s11
	v_lshl_add_u64 v[8:9], s[4:5], 0, v[2:3]
	v_lshlrev_b32_e32 v6, 2, v76
	v_mov_b32_e32 v7, v3
	v_lshl_add_u64 v[8:9], v[8:9], 0, s[48:49]
	s_lshl_b32 s48, s8, 7
	v_lshlrev_b32_e32 v4, 1, v76
	v_mov_b32_e32 v5, v3
	v_lshl_add_u64 v[12:13], v[8:9], 0, v[6:7]
	v_lshl_add_u64 v[6:7], v[8:9], 0, s[48:49]
	s_mov_b32 s4, 0xa201000
	v_lshl_add_u64 v[10:11], v[6:7], 0, v[4:5]
	v_add_co_u32_e32 v4, vcc, s4, v12
	s_mov_b32 s4, 0xe201000
	s_nop 0
	v_addc_co_u32_e32 v5, vcc, 0, v13, vcc
	v_add_co_u32_e32 v14, vcc, s4, v12
	s_mov_b32 s4, 0x12201000
	s_nop 0
	v_addc_co_u32_e32 v15, vcc, 0, v13, vcc
	v_add_co_u32_e32 v6, vcc, s4, v10
	s_mov_b32 s4, 0xa203000
	s_nop 0
	v_addc_co_u32_e32 v7, vcc, 0, v11, vcc
	v_add_co_u32_e32 v24, vcc, s4, v12
	s_mov_b32 s4, 0xe203000
	s_nop 0
	v_addc_co_u32_e32 v25, vcc, 0, v13, vcc
	v_add_co_u32_e32 v20, vcc, s4, v12
	s_mov_b32 s4, 0x12203000
	s_nop 0
	v_addc_co_u32_e32 v21, vcc, 0, v13, vcc
	v_add_co_u32_e32 v8, vcc, s4, v10
	s_mov_b32 s4, 0xa205000
	s_nop 0
	v_addc_co_u32_e32 v9, vcc, 0, v11, vcc
	v_add_co_u32_e32 v28, vcc, s4, v12
	s_mov_b32 s4, 0xe205000
	s_nop 0
	v_addc_co_u32_e32 v29, vcc, 0, v13, vcc
	v_add_co_u32_e32 v22, vcc, s4, v12
	s_mov_b32 s4, 0x12205000
	s_nop 0
	v_addc_co_u32_e32 v23, vcc, 0, v13, vcc
	v_add_co_u32_e32 v16, vcc, s4, v10
	s_mov_b32 s4, 0xa207000
	s_nop 0
	v_addc_co_u32_e32 v17, vcc, 0, v11, vcc
	v_add_co_u32_e32 v18, vcc, s4, v12
	s_mov_b32 s4, 0xe207000
	s_nop 0
	v_addc_co_u32_e32 v19, vcc, 0, v13, vcc
	v_add_co_u32_e32 v32, vcc, s4, v12
	s_mov_b32 s4, 0x12207000
	s_nop 0
	v_addc_co_u32_e32 v33, vcc, 0, v13, vcc
	v_add_co_u32_e32 v26, vcc, s4, v10
	s_mov_b32 s4, 0xa221000
	s_nop 0
	v_addc_co_u32_e32 v27, vcc, 0, v11, vcc
	v_add_co_u32_e32 v30, vcc, s4, v12
	s_mov_b32 s4, 0xe221000
	s_nop 0
	v_addc_co_u32_e32 v31, vcc, 0, v13, vcc
	v_add_co_u32_e32 v34, vcc, s4, v12
	s_mov_b32 s4, 0x12221000
	s_nop 0
	v_addc_co_u32_e32 v35, vcc, 0, v13, vcc
	v_add_co_u32_e32 v36, vcc, s4, v10
	s_mov_b32 s4, 0xa223000
	s_nop 0
	v_addc_co_u32_e32 v37, vcc, 0, v11, vcc
	v_add_co_u32_e32 v38, vcc, s4, v12
	s_mov_b32 s4, 0xe223000
	s_nop 0
	v_addc_co_u32_e32 v39, vcc, 0, v13, vcc
	v_add_co_u32_e32 v40, vcc, s4, v12
	s_mov_b32 s4, 0x12223000
	s_nop 0
	v_addc_co_u32_e32 v41, vcc, 0, v13, vcc
	v_add_co_u32_e32 v42, vcc, s4, v10
	s_mov_b32 s4, 0xa225000
	s_nop 0
	v_addc_co_u32_e32 v43, vcc, 0, v11, vcc
	v_add_co_u32_e32 v44, vcc, s4, v12
	s_mov_b32 s4, 0xe225000
	s_nop 0
	v_addc_co_u32_e32 v45, vcc, 0, v13, vcc
	v_add_co_u32_e32 v46, vcc, s4, v12
	s_mov_b32 s4, 0x12225000
	s_nop 0
	v_addc_co_u32_e32 v47, vcc, 0, v13, vcc
	v_add_co_u32_e32 v48, vcc, s4, v10
	s_mov_b32 s4, 0xa227000
	s_nop 0
	v_addc_co_u32_e32 v49, vcc, 0, v11, vcc
; #define LAS __attribute__((address_space(3)))
; template <int SET> DI void h_load8(unsigned (&CR)[72], const bf16_t* qp, const bf16_t* fp, const bf16_t* ip, int c) {
; #pragma unroll
;     for (int j = 0; j < 8; ++j) { const size_t ro = (size_t)(32 * c + j) * D; CR[24 * SET + j] = *(const unsigned*)(qp + ro); CR[24 * SET + 8 + j] = *(const unsigned*)(fp + ro); CR[24 * SET + 16 + j] = ip[ro]; }
; }
; template <int SET> DI void h_totals8(const unsigned (&CR)[72], LAS unsigned char* buf, int tgp, int k2) {
;     float lo = 0.f, hi = 0.f;
; #pragma unroll
;     for (int j = 0; j < 8; ++j) { lo += bflo(CR[24 * SET + 8 + j]); hi += bfhi(CR[24 * SET + 8 + j]); }
;     *(LAS f32x2_t*)(buf + H_TOT + (tgp * 128 + 2 * k2) * 4) = (f32x2_t){lo, hi};
; }
; DI void p2_hgrn_roles(Frame& F, ArgsP A) {
;     ...
;             h_load8<0>(CR, qp, fp, ip, 0); h_load8<1>(CR, qp, fp, ip, 1); h_load8<2>(CR, qp, fp, ip, 2); h_totals8<0>(CR, lds, tgp, k2);
	v_add_co_u32_e32 v50, vcc, s4, v12
	s_mov_b32 s4, 0xe227000
	s_nop 0
	v_addc_co_u32_e32 v51, vcc, 0, v13, vcc
	v_add_co_u32_e32 v52, vcc, s4, v12
	s_mov_b32 s4, 0x12227000
	s_nop 0
	v_addc_co_u32_e32 v53, vcc, 0, v13, vcc
	v_add_co_u32_e32 v54, vcc, s4, v10
	s_mov_b32 s4, 0xa241000
	s_nop 0
	v_addc_co_u32_e32 v55, vcc, 0, v11, vcc
	v_add_co_u32_e32 v56, vcc, s4, v12
	s_mov_b32 s4, 0xe241000
	s_nop 0
	v_addc_co_u32_e32 v57, vcc, 0, v13, vcc
	v_add_co_u32_e32 v58, vcc, s4, v12
	s_mov_b32 s4, 0x12241000
	s_nop 0
	v_addc_co_u32_e32 v59, vcc, 0, v13, vcc
	v_add_co_u32_e32 v60, vcc, s4, v10
	s_mov_b32 s4, 0xa243000
	s_nop 0
	v_addc_co_u32_e32 v61, vcc, 0, v11, vcc
	v_add_co_u32_e32 v62, vcc, s4, v12
	global_load_dword v123, v[24:25], off offset:-4096 nt
	global_load_dword v143, v[24:25], off nt
	global_load_dword v121, v[14:15], off offset:-4096 nt
	global_load_ushort v185, v[6:7], off nt
	global_load_dword v122, v[14:15], off nt
	global_load_dword v124, v[4:5], off nt
	v_addc_co_u32_e32 v63, vcc, 0, v13, vcc
	v_add_co_u32_e32 v64, vcc, s74, v12
	global_load_dword v145, v[28:29], off offset:-4096 nt
	global_load_dword v164, v[22:23], off nt
	global_load_dword v159, v[28:29], off nt
	global_load_dword v133, v[20:21], off offset:-4096 nt
	global_load_ushort v186, v[8:9], off nt
	global_load_dword v144, v[20:21], off nt
	v_addc_co_u32_e32 v65, vcc, 0, v13, vcc
	v_add_co_u32_e32 v66, vcc, s75, v10
	global_load_dword v150, v[22:23], off offset:-4096 nt
	s_nop 0
	v_addc_co_u32_e32 v67, vcc, 0, v11, vcc
	v_add_co_u32_e32 v68, vcc, s76, v12
	global_load_dword v171, v[32:33], off offset:-4096 nt
	global_load_ushort v187, v[26:27], off nt
	global_load_dword v174, v[32:33], off nt
	global_load_dword v177, v[18:19], off nt
	v_addc_co_u32_e32 v69, vcc, 0, v13, vcc
	v_add_co_u32_e32 v70, vcc, s77, v12
	v_lshlrev_b32_e32 v2, 9, v77
	s_nop 0
	v_addc_co_u32_e32 v71, vcc, 0, v13, vcc
	v_add_co_u32_e32 v72, vcc, s79, v12
	s_waitcnt vmcnt(14)
	v_lshlrev_b32_e32 v14, 16, v121
	v_addc_co_u32_e32 v73, vcc, 0, v13, vcc
	v_add_co_u32_e32 v12, vcc, s80, v12
	v_and_b32_e32 v15, 0xffff0000, v121
	s_nop 0
	v_addc_co_u32_e32 v13, vcc, 0, v13, vcc
	v_add_co_u32_e32 v74, vcc, s78, v10
	v_pk_add_f32 v[14:15], v[14:15], 0 op_sel_hi:[1,0]
	s_nop 0
	v_addc_co_u32_e32 v75, vcc, 0, v11, vcc
	v_add_co_u32_e32 v10, vcc, s81, v10
	s_waitcnt vmcnt(12)
	v_lshlrev_b32_e32 v24, 16, v122
	v_addc_co_u32_e32 v11, vcc, 0, v11, vcc
	global_load_ushort v188, v[8:9], off offset:-4096 nt
	global_load_ushort v189, v[6:7], off offset:-4096 nt
	global_load_dword v142, v[4:5], off offset:-4096 nt
	global_load_ushort v190, v[26:27], off offset:-4096 nt
	global_load_ushort v191, v[16:17], off offset:-4096 nt
	global_load_ushort v192, v[16:17], off nt
	global_load_dword v184, v[18:19], off offset:-4096 nt
	global_load_ushort v126, v[36:37], off offset:-4096 nt
	global_load_ushort v128, v[36:37], off nt
	global_load_dword v136, v[38:39], off offset:-4096 nt
	global_load_dword v152, v[38:39], off nt
	global_load_dword v130, v[34:35], off offset:-4096 nt
	global_load_dword v132, v[34:35], off nt
	global_load_dword v137, v[30:31], off offset:-4096 nt
	global_load_dword v139, v[30:31], off nt
	global_load_ushort v147, v[42:43], off offset:-4096 nt
	global_load_ushort v149, v[42:43], off nt
	global_load_dword v156, v[46:47], off offset:-4096 nt
	global_load_dword v168, v[46:47], off nt
	global_load_dword v161, v[44:45], off offset:-4096 nt
	global_load_dword v163, v[44:45], off nt
	global_load_dword v141, v[40:41], off offset:-4096 nt
	global_load_dword v158, v[40:41], off nt
	global_load_ushort v154, v[48:49], off offset:-4096 nt
	global_load_ushort v166, v[48:49], off nt
	global_load_ushort v170, v[54:55], off offset:-4096 nt
	global_load_ushort v181, v[54:55], off nt
	global_load_dword v173, v[52:53], off offset:-4096 nt
	global_load_dword v176, v[52:53], off nt
	global_load_dword v179, v[50:51], off offset:-4096 nt
	global_load_dword v183, v[50:51], off nt
	global_load_ushort v125, v[60:61], off offset:-4096 nt
	global_load_ushort v127, v[60:61], off nt
	global_load_dword v134, v[62:63], off offset:-4096 nt
	global_load_dword v151, v[62:63], off nt
	global_load_dword v129, v[58:59], off offset:-4096 nt
	global_load_dword v131, v[58:59], off nt
	global_load_dword v135, v[56:57], off offset:-4096 nt
	global_load_dword v138, v[56:57], off nt
	global_load_ushort v146, v[66:67], off offset:-4096 nt
	global_load_ushort v148, v[66:67], off nt
	global_load_dword v155, v[70:71], off offset:-4096 nt
	global_load_dword v167, v[70:71], off nt
	global_load_dword v160, v[68:69], off offset:-4096 nt
	global_load_dword v162, v[68:69], off nt
	global_load_dword v140, v[64:65], off offset:-4096 nt
	global_load_dword v157, v[64:65], off nt
	global_load_ushort v153, v[74:75], off offset:-4096 nt
	global_load_ushort v165, v[74:75], off nt
	global_load_ushort v169, v[10:11], off offset:-4096 nt
	global_load_ushort v180, v[10:11], off nt
	global_load_dword v172, v[12:13], off offset:-4096 nt
	global_load_dword v175, v[12:13], off nt
	global_load_dword v178, v[72:73], off offset:-4096 nt
	global_load_dword v182, v[72:73], off nt
	v_and_b32_e32 v25, 0xffff0000, v122
	v_pk_add_f32 v[14:15], v[14:15], v[24:25]
	s_waitcnt vmcnt(62)
	v_lshlrev_b32_e32 v20, 16, v133
	v_and_b32_e32 v21, 0xffff0000, v133
	v_pk_add_f32 v[14:15], v[14:15], v[20:21]
	s_waitcnt vmcnt(60)
	v_lshlrev_b32_e32 v20, 16, v144
	v_and_b32_e32 v21, 0xffff0000, v144
	v_pk_add_f32 v[14:15], v[14:15], v[20:21]
	s_waitcnt vmcnt(59)
	v_lshlrev_b32_e32 v20, 16, v150
	v_and_b32_e32 v21, 0xffff0000, v150
	v_pk_add_f32 v[14:15], v[14:15], v[20:21]
	v_lshlrev_b32_e32 v20, 16, v164
	v_and_b32_e32 v21, 0xffff0000, v164
	v_pk_add_f32 v[14:15], v[14:15], v[20:21]
	s_waitcnt vmcnt(58)
	v_lshlrev_b32_e32 v20, 16, v171
	v_and_b32_e32 v21, 0xffff0000, v171
	v_pk_add_f32 v[14:15], v[14:15], v[20:21]
	s_waitcnt vmcnt(56)
	v_lshlrev_b32_e32 v20, 16, v174
	v_and_b32_e32 v21, 0xffff0000, v174
	v_lshlrev_b32_e32 v4, 3, v76
	v_pk_add_f32 v[14:15], v[14:15], v[20:21]
	v_add3_u32 v2, 0, v2, v4
	ds_write_b64 v2, v[14:15] offset:41984

; #define LAS __attribute__((address_space(3)))
; DI unsigned pk2(float lo, float hi) { return cvtpk_s(lo, hi); }
; template <int SET> DI void h_load8(unsigned (&CR)[72], const bf16_t* qp, const bf16_t* fp, const bf16_t* ip, int c) {
; #pragma unroll
;     for (int j = 0; j < 8; ++j) { const size_t ro = (size_t)(32 * c + j) * D; CR[24 * SET + j] = *(const unsigned*)(qp + ro); CR[24 * SET + 8 + j] = *(const unsigned*)(fp + ro); CR[24 * SET + 16 + j] = ip[ro]; }
; }
; DI void h_reduce_store2(LAS unsigned char* red, bf16_t* op, int c, int pt) {
; #pragma unroll
;     for (int s2 = 0; s2 < 2; ++s2) {
;         const int s = pt + 256 * s2, t = s >> 4, c4 = s & 15;
;         const f32x4 a = *(const LAS f32x4*)(red + ((0 * 32 + t) * 64 + 4 * c4) * 4), b2 = *(const LAS f32x4*)(red + ((1 * 32 + t) * 64 + 4 * c4) * 4);
;         const f32x4 sm = a + b2;
;         u32x2 w; w.x = pk2(sm[0], sm[1]); w.y = pk2(sm[2], sm[3]);
;         *(u32x2*)(op + (size_t)(32 * c + t) * D + 4 * c4) = w;
;     }
; }
.LBB0_414:
	s_andn2_b64 vcc, exec, s[4:5]
	s_cbranch_vccnz .LBB0_420
	v_mov_b32_e32 v4, v0
	s_load_dwordx2 s[4:5], s[40:41], 0x98
	s_waitcnt lgkmcnt(0)
	s_add_u32 s98, s4, s54
	s_addc_u32 s99, s5, s55
	s_add_u32 s98, s98, s56
	s_addc_u32 s99, s99, s57
	s_add_u32 s98, s98, 0xa260000
	s_addc_u32 s99, s99, 0
	v_lshlrev_b32_e32 v2, 9, v4
	v_and_b32_e32 v6, 63, v4
	v_and_b32_e32 v5, 0x18000, v2
	v_lshl_or_b32 v2, v6, 2, v5
	v_lshl_or_b32 v2, v6, 1, v5
	global_load_dword v142, v200, s[98:99] nt
	global_load_dword v124, v201, s[98:99] nt
	global_load_dword v123, v202, s[98:99] nt
	global_load_dword v143, v203, s[98:99] nt
	global_load_dword v145, v204, s[98:99] nt
	global_load_dword v159, v205, s[98:99] nt
	global_load_dword v184, v206, s[98:99] nt
	global_load_dword v177, v207, s[98:99] nt
	s_add_u32 s98, s98, 0x4000000
	s_addc_u32 s99, s99, 0
	global_load_dword v121, v200, s[98:99] nt
	global_load_dword v122, v201, s[98:99] nt
	global_load_dword v133, v202, s[98:99] nt
	global_load_dword v144, v203, s[98:99] nt
	global_load_dword v150, v204, s[98:99] nt
	global_load_dword v164, v205, s[98:99] nt
	global_load_dword v171, v206, s[98:99] nt
	global_load_dword v174, v207, s[98:99] nt
	s_add_u32 s98, s98, 0x4000000
	s_addc_u32 s99, s99, 0
	global_load_ushort v189, v208, s[98:99] nt
	global_load_ushort v185, v209, s[98:99] nt
	global_load_ushort v188, v210, s[98:99] nt
	global_load_ushort v186, v211, s[98:99] nt
	global_load_ushort v191, v212, s[98:99] nt
	global_load_ushort v192, v213, s[98:99] nt
	global_load_ushort v190, v214, s[98:99] nt
	global_load_ushort v187, v215, s[98:99] nt
	s_cmp_eq_u32 s56, 0
	s_cbranch_scc1 .LBB0_417
	s_and_b32 s6, s38, 0x4000
	s_add_i32 s6, s6, 0
	s_add_i32 s8, s6, 0x16800
	s_lshl_b64 s[6:7], s[52:53], 1
	s_add_u32 s4, s4, s6
	s_addc_u32 s5, s5, s7
	s_lshl_b32 s6, s96, 1
	v_lshlrev_b32_sdwa v2, v1, v4 dst_sel:DWORD dst_unused:UNUSED_PAD src0_sel:DWORD src1_sel:BYTE_0
	s_add_u32 s4, s4, s6
	v_and_b32_e32 v2, 60, v2
	v_lshrrev_b32_sdwa v15, v118, v4 dst_sel:DWORD dst_unused:UNUSED_PAD src0_sel:DWORD src1_sel:BYTE_0
	s_addc_u32 s5, s5, 0
	s_lshl_b32 s6, s48, 1
	v_lshlrev_b32_e32 v5, 2, v2
	v_lshlrev_b32_e32 v16, 8, v15
	s_add_u32 s4, s4, s6
	v_add3_u32 v5, s8, v5, v16
	s_addc_u32 s5, s5, 0
	v_lshlrev_b32_e32 v2, 1, v2
	ds_read_b128 v[16:19], v5
	ds_read_b128 v[20:23], v5 offset:8192
	v_lshl_add_u64 v[24:25], s[4:5], 0, v[2:3]
	v_lshl_add_u64 v[32:33], v[24:25], 0, s[50:51]
	ds_read_b128 v[24:27], v5 offset:4096
	ds_read_b128 v[28:31], v5 offset:12288
	v_lshl_add_u32 v2, v15, 11, s97
	s_waitcnt lgkmcnt(2)
	v_pk_add_f32 v[18:19], v[18:19], v[22:23]
	v_pk_add_f32 v[16:17], v[16:17], v[20:21]
	s_nop 0
	v_cvt_pk_bf16_f32 v16, v16, v17
	v_cvt_pk_bf16_f32 v17, v18, v19
	v_lshl_add_u64 v[18:19], v[2:3], 1, v[32:33]
	global_store_dwordx2 v[18:19], v[16:17], off
	s_waitcnt lgkmcnt(0)
	v_pk_add_f32 v[16:17], v[26:27], v[30:31]
	v_pk_add_f32 v[18:19], v[24:25], v[28:29]
	v_add_u32_e32 v2, 0x8000, v2
	v_cvt_pk_bf16_f32 v18, v18, v19
	v_cvt_pk_bf16_f32 v19, v16, v17
	v_lshl_add_u64 v[16:17], v[2:3], 1, v[32:33]
	global_store_dwordx2 v[16:17], v[18:19], off

; #define LAS __attribute__((address_space(3)))
; DI int opaque_tid() { int t = threadIdx.x; asm volatile("" : "+v"(t)); return t; }
; template <int SET> DI void h_load8(unsigned (&CR)[72], const bf16_t* qp, const bf16_t* fp, const bf16_t* ip, int c) {
; #pragma unroll
;     for (int j = 0; j < 8; ++j) { const size_t ro = (size_t)(32 * c + j) * D; CR[24 * SET + j] = *(const unsigned*)(qp + ro); CR[24 * SET + 8 + j] = *(const unsigned*)(fp + ro); CR[24 * SET + 16 + j] = ip[ro]; }
; }
; template <int RF, int RN, int RNN> DI void h_prep_step(unsigned (&CR)[72], ArgsP A, LAS unsigned char* lds, int cc, size_t rb, int h, int vhalf) {
;     const int pt = opaque_tid() & 255, k2 = pt & 63, tgp = pt >> 6, v64 = pt & 63;
;     const bf16_t* QA = (const bf16_t*)(A->ws + WS_QA); const bf16_t* LF = (const bf16_t*)(A->ws + WS_LF); const bf16_t* IA = (const bf16_t*)(A->ws + WS_IA); bf16_t* OH = (bf16_t*)(A->ws + WS_OH);
;     if (cc + 3 < 64) {
;         const bf16_t* qp = QA + rb + (size_t)(8 * tgp) * D + h * 128 + 2 * k2; const bf16_t* fp = LF + rb + (size_t)(8 * tgp) * D + h * 128 + 2 * k2;
;         const bf16_t* ip = IA + rb + (size_t)(8 * tgp) * D + h * 128 + vhalf * 64 + v64;
;         h_load8<RF>(CR, qp, fp, ip, cc + 3);
.LBB0_422:
	s_andn2_b64 vcc, exec, s[4:5]
	s_cbranch_vccnz .LBB0_428
	v_mov_b32_e32 v36, v0
	s_load_dwordx2 s[4:5], s[40:41], 0x98
	s_cmp_gt_u32 s39, 59
	v_and_b32_e32 v38, 63, v36
	s_cbranch_scc1 .Lp2_skip_b
	s_waitcnt lgkmcnt(0)
	s_add_u32 s98, s4, s54
	s_addc_u32 s99, s5, s55
	s_add_u32 s98, s98, s56
	s_addc_u32 s99, s99, s57
	s_add_u32 s98, s98, 0xa280000
	s_addc_u32 s99, s99, 0
	v_lshlrev_b32_e32 v2, 9, v36
	v_and_b32_e32 v37, 0x18000, v2
	v_lshl_or_b32 v2, v38, 2, v37
	v_lshl_or_b32 v2, v38, 1, v37
	global_load_dword v137, v200, s[98:99] nt
	global_load_dword v139, v201, s[98:99] nt
	global_load_dword v136, v202, s[98:99] nt
	global_load_dword v152, v203, s[98:99] nt
	global_load_dword v161, v204, s[98:99] nt
	global_load_dword v163, v205, s[98:99] nt
	global_load_dword v179, v206, s[98:99] nt
	global_load_dword v183, v207, s[98:99] nt
	s_add_u32 s98, s98, 0x4000000
	s_addc_u32 s99, s99, 0
	global_load_dword v130, v200, s[98:99] nt
	global_load_dword v132, v201, s[98:99] nt
	global_load_dword v141, v202, s[98:99] nt
	global_load_dword v158, v203, s[98:99] nt
	global_load_dword v156, v204, s[98:99] nt
	global_load_dword v168, v205, s[98:99] nt
	global_load_dword v173, v206, s[98:99] nt
	global_load_dword v176, v207, s[98:99] nt
	s_add_u32 s98, s98, 0x4000000
	s_addc_u32 s99, s99, 0
	global_load_ushort v126, v208, s[98:99] nt
	global_load_ushort v128, v209, s[98:99] nt
	global_load_ushort v147, v210, s[98:99] nt
	global_load_ushort v149, v211, s[98:99] nt
	global_load_ushort v154, v212, s[98:99] nt
	global_load_ushort v166, v213, s[98:99] nt
	global_load_ushort v170, v214, s[98:99] nt
	global_load_ushort v181, v215, s[98:99] nt

; #define LAS __attribute__((address_space(3)))
; DI int opaque_tid() { int t = threadIdx.x; asm volatile("" : "+v"(t)); return t; }
; template <int SET> DI void h_load8(unsigned (&CR)[72], const bf16_t* qp, const bf16_t* fp, const bf16_t* ip, int c) {
; #pragma unroll
;     for (int j = 0; j < 8; ++j) { const size_t ro = (size_t)(32 * c + j) * D; CR[24 * SET + j] = *(const unsigned*)(qp + ro); CR[24 * SET + 8 + j] = *(const unsigned*)(fp + ro); CR[24 * SET + 16 + j] = ip[ro]; }
; }
; template <int RF, int RN, int RNN> DI void h_prep_step(unsigned (&CR)[72], ArgsP A, LAS unsigned char* lds, int cc, size_t rb, int h, int vhalf) {
;     const int pt = opaque_tid() & 255, k2 = pt & 63, tgp = pt >> 6, v64 = pt & 63;
;     const bf16_t* QA = (const bf16_t*)(A->ws + WS_QA); const bf16_t* LF = (const bf16_t*)(A->ws + WS_LF); const bf16_t* IA = (const bf16_t*)(A->ws + WS_IA); bf16_t* OH = (bf16_t*)(A->ws + WS_OH);
;     if (cc + 3 < 64) {
;         const bf16_t* qp = QA + rb + (size_t)(8 * tgp) * D + h * 128 + 2 * k2; const bf16_t* fp = LF + rb + (size_t)(8 * tgp) * D + h * 128 + 2 * k2;
;         const bf16_t* ip = IA + rb + (size_t)(8 * tgp) * D + h * 128 + vhalf * 64 + v64;
;         h_load8<RF>(CR, qp, fp, ip, cc + 3);
.LBB0_431:
	s_andn2_b64 vcc, exec, s[4:5]
	s_cbranch_vccnz .LBB0_438
	v_mov_b32_e32 v36, v0
	s_load_dwordx2 s[4:5], s[40:41], 0x98
	s_cmp_gt_u32 s39, 58
	v_and_b32_e32 v38, 63, v36
	s_cbranch_scc1 .Lp2_skip_c
	s_waitcnt lgkmcnt(0)
	s_add_u32 s98, s4, s54
	s_addc_u32 s99, s5, s55
	s_add_u32 s98, s98, s56
	s_addc_u32 s99, s99, s57
	s_add_u32 s98, s98, 0xa2a0000
	s_addc_u32 s99, s99, 0
	v_lshlrev_b32_e32 v2, 9, v36
	v_and_b32_e32 v37, 0x18000, v2
	v_lshl_or_b32 v2, v38, 2, v37
	v_lshl_or_b32 v2, v38, 1, v37
	global_load_dword v135, v200, s[98:99] nt
	global_load_dword v138, v201, s[98:99] nt
	global_load_dword v134, v202, s[98:99] nt
	global_load_dword v151, v203, s[98:99] nt
	global_load_dword v160, v204, s[98:99] nt
	global_load_dword v162, v205, s[98:99] nt
	global_load_dword v178, v206, s[98:99] nt
	global_load_dword v182, v207, s[98:99] nt
	s_add_u32 s98, s98, 0x4000000
	s_addc_u32 s99, s99, 0
	global_load_dword v129, v200, s[98:99] nt
	global_load_dword v131, v201, s[98:99] nt
	global_load_dword v140, v202, s[98:99] nt
	global_load_dword v157, v203, s[98:99] nt
	global_load_dword v155, v204, s[98:99] nt
	global_load_dword v167, v205, s[98:99] nt
	global_load_dword v172, v206, s[98:99] nt
	global_load_dword v175, v207, s[98:99] nt
	s_add_u32 s98, s98, 0x4000000
	s_addc_u32 s99, s99, 0
	global_load_ushort v125, v208, s[98:99] nt
	global_load_ushort v127, v209, s[98:99] nt
	global_load_ushort v146, v210, s[98:99] nt
	global_load_ushort v148, v211, s[98:99] nt
	global_load_ushort v153, v212, s[98:99] nt
	global_load_ushort v165, v213, s[98:99] nt
	global_load_ushort v169, v214, s[98:99] nt
	global_load_ushort v180, v215, s[98:99] nt
